# P9 K-loop LDS-DMA re-phased: both A half-tiles of a K-tile staged in the SP1 load interval, both B half-tiles in SP2 (4 pieces per load interval instead of 2/6), waits vmcnt 8/6/8/6
# speedup vs baseline: 1.0080x; 1.0080x over previous
; #define PG8_STAGE(bufoff, gbase, voff) do { PG8_GLDS((const char*)(gbase), (voff)[0], ldsb + (bufoff)); PG8_GLDS((const char*)(gbase), (voff)[1], ldsb + (bufoff) + 8192u); } while (0)
; #define PG8_STAGEA(bufoff, gbase, o0, o1) do { PG8_GLDS((const char*)(gbase), (o0), ldsb + (bufoff)); PG8_GLDS((const char*)(gbase), (o1), ldsb + (bufoff) + 8192u); } while (0)
; template <class Epi, class Sched, bool F8 = false, bool PF = false, bool I8 = false, int PID = -1>
; __device__ __forceinline__ void gemm_phase(LAS unsigned char* lds, LAS unsigned char* xlds, const int RP, const int RPB, const int nt, const Sched& S, const Epi& E, const int stagger_ticks) {
;     ...
;             const char* a2 = last ? nA : cA + (size_t)(t + 2) * kstep; const char* b2 = last ? nB : cB + (size_t)(t + 2) * kstep;
;             const char* a3 = a2 + kstep; const char* b3 = b2 + kstep;
;             if constexpr (PF) { const char* pfa = (t + 4 < nt) ? cA + (size_t)(t + 4) * kstep : nA + (size_t)(t + 4 - nt) * kstep;
;                 asm volatile("s_mov_b32 m0, %2\n\ts_nop 0\n\tglobal_load_lds_dword %0, %1" :: "v"(voffP), "s"(pfa), "s"(ldsP) : "memory", "m0"); }
;             const bool relax = (Epi::RELAX > 0) && (t == 0) && epi_ran;
;             PG8_LDB(B0, 0, 0); PG8_LDB(B1, 0, 1); PG8_SCHED; PG8_LDA(At, 0, 0); PG8_STAGEA1(PG8_SA(1, 1), a1);
;             if (Sched::GATHER) { if (last) { const u32x4 nv = *nslot; vA0 = nv.x; vA1 = nv.y; vA2 = nv.z; vA3 = nv.w; } }
;             PG8_WAIT_VX(); PG8_WAIT_L(0); PG8_BAR; PG8_MMA(0, 0, At, B0); PG8_MMA(0, 1, At, B1); PG8_BAR; PG8_SCHED;
;             if constexpr (Epi::BIAS_DMA) { if (t == 0 && has_next) E.bias_dma(nxt, xlds + 8192 + ((ui + 1) & 1) * Epi::BIAS_STRIDE, wid, lane); }
;             PG8_LDA(At, 0, 1); PG8_STAGE(PG8_SB(0, 0), b2, voffB); PG8_STAGE(PG8_SB(0, 1), b2 + hstepB, voffB); PG8_STAGEA(PG8_SA(0, 0), a2, vA0, vA1);
;             PG8_WAIT_VX(); PG8_WAIT_L(0); PG8_BAR; PG8_MMA(1, 0, At, B0); PG8_MMA(1, 1, At, B1); PG8_BAR; PG8_SCHED;
;             PG8_LDB(B0, 1, 0); PG8_LDB(B1, 1, 1); PG8_SCHED; PG8_LDA(At, 1, 0); PG8_STAGEA1(PG8_SA(0, 1), a2);
;             PG8_WAIT_VR(); PG8_WAIT_L(0); PG8_BAR; PG8_MMA(0, 0, At, B0); PG8_MMA(0, 1, At, B1); PG8_BAR; PG8_SCHED;
;             PG8_LDA(At, 1, 1); PG8_STAGE(PG8_SB(1, 0), b3, voffB); PG8_STAGE(PG8_SB(1, 1), b3 + hstepB, voffB); PG8_STAGEA(PG8_SA(1, 0), a3, vA0, vA1);
.LBB0_1062:
	s_add_u32 s30, s26, 0xfffe0080
	s_addc_u32 s31, s27, -1
	s_cmp_eq_u32 s73, 4
	s_cselect_b32 s38, s6, s30
	s_cselect_b32 s39, s7, s31
	s_cselect_b32 s34, s8, s25
	s_cselect_b32 s35, s9, s71
	s_add_u32 s30, s38, 0x80
	s_addc_u32 s31, s39, 0
	s_add_u32 s36, s34, 0x80
	s_addc_u32 s37, s35, 0
	ds_read_b128 v[170:173], v169 offset:16384
	ds_read_b128 v[174:177], v169 offset:17408
	ds_read_b128 v[178:181], v169 offset:18432
	ds_read_b128 v[182:185], v169 offset:19456
	ds_read_b128 v[186:189], v169 offset:20480
	ds_read_b128 v[190:193], v169 offset:21504
	ds_read_b128 v[194:197], v169 offset:22528
	ds_read_b128 v[198:201], v169 offset:23552
	s_add_i32 s75, s74, 0x10000
	s_mov_b32 m0, s75
	s_nop 0
	global_load_lds_dwordx4 v166, s[34:35]
	s_add_i32 s75, s74, 0x12000
	s_mov_b32 m0, s75
	s_nop 0
	global_load_lds_dwordx4 v167, s[34:35]
	s_add_u32 s76, s34, 0x2000
	s_addc_u32 s77, s35, 0
	s_add_i32 s75, s74, 0x14000
	s_mov_b32 m0, s75
	s_nop 0
	global_load_lds_dwordx4 v166, s[76:77]
	s_add_i32 s75, s74, 0x16000
	s_mov_b32 m0, s75
	s_nop 0
	global_load_lds_dwordx4 v167, s[76:77]
	s_waitcnt vmcnt(6)
	s_waitcnt lgkmcnt(0)
	s_barrier
	s_setprio 1
	s_waitcnt lgkmcnt(6)
	v_mfma_f32_16x16x128_f8f6f4 v[86:89], v[2:9], v[170:177], v[86:89]
	v_mfma_f32_16x16x128_f8f6f4 v[82:85], v[10:17], v[170:177], v[82:85]
	s_waitcnt lgkmcnt(4)
	v_mfma_f32_16x16x128_f8f6f4 v[70:73], v[2:9], v[178:185], v[70:73]
	v_mfma_f32_16x16x128_f8f6f4 v[66:69], v[10:17], v[178:185], v[66:69]
	s_waitcnt lgkmcnt(2)
	v_mfma_f32_16x16x128_f8f6f4 v[202:205], v[2:9], v[186:193], v[54:57]
	v_mfma_f32_16x16x128_f8f6f4 v[206:209], v[10:17], v[186:193], v[50:53]
	s_waitcnt lgkmcnt(0)
	v_mfma_f32_16x16x128_f8f6f4 v[210:213], v[2:9], v[194:201], v[38:41]
	v_mfma_f32_16x16x128_f8f6f4 v[214:217], v[10:17], v[194:201], v[34:37]
	v_mfma_f32_16x16x128_f8f6f4 v[94:97], v[18:25], v[170:177], v[94:97]
	v_mfma_f32_16x16x128_f8f6f4 v[90:93], v[26:33], v[170:177], v[90:93]
	v_mfma_f32_16x16x128_f8f6f4 v[78:81], v[18:25], v[178:185], v[78:81]
	v_mfma_f32_16x16x128_f8f6f4 v[74:77], v[26:33], v[178:185], v[74:77]
	v_mfma_f32_16x16x128_f8f6f4 v[218:221], v[18:25], v[186:193], v[62:65]
	v_mfma_f32_16x16x128_f8f6f4 v[186:189], v[26:33], v[186:193], v[58:61]
	v_mfma_f32_16x16x128_f8f6f4 v[190:193], v[18:25], v[194:201], v[46:49]
	v_mfma_f32_16x16x128_f8f6f4 v[194:197], v[26:33], v[194:201], v[42:45]
	s_setprio 0
	s_barrier
	s_add_i32 s75, s74, 0x2000
	s_mov_b32 m0, s74
	s_nop 0
	global_load_lds_dwordx4 v164, s[38:39]
	s_nop 0
	s_mov_b32 m0, s75
	s_nop 0
	global_load_lds_dwordx4 v165, s[38:39]
	v_add_u32_e32 v14, 0x18000, v168
	v_add_u32_e32 v30, 0x1c000, v168
	ds_read_b128 v[2:5], v14
	ds_read_b128 v[6:9], v14 offset:1024
	ds_read_b128 v[10:13], v14 offset:2048
	ds_read_b128 v[14:17], v14 offset:3072
	ds_read_b128 v[18:21], v30
	ds_read_b128 v[22:25], v30 offset:1024
	ds_read_b128 v[26:29], v30 offset:2048
	ds_read_b128 v[30:33], v30 offset:3072
	ds_read_b128 v[34:37], v169 offset:32768
	ds_read_b128 v[38:41], v169 offset:33792
	ds_read_b128 v[42:45], v169 offset:34816
	ds_read_b128 v[46:49], v169 offset:35840
	ds_read_b128 v[50:53], v169 offset:36864
	ds_read_b128 v[54:57], v169 offset:37888
	ds_read_b128 v[58:61], v169 offset:38912
	ds_read_b128 v[62:65], v169 offset:39936
	s_add_u32 s38, s38, 0x20000
	s_addc_u32 s39, s39, 0
	s_add_i32 s75, s74, 0x4000
	s_mov_b32 m0, s75
	s_nop 0
	global_load_lds_dwordx4 v164, s[38:39]
	s_add_i32 s75, s74, 0x6000
	s_mov_b32 m0, s75
	s_nop 0
	global_load_lds_dwordx4 v165, s[38:39]
	s_waitcnt vmcnt(8)
	s_waitcnt lgkmcnt(0)
	s_barrier
	s_setprio 1
	s_waitcnt lgkmcnt(6)
	v_mfma_f32_16x16x128_f8f6f4 v[150:153], v[2:9], v[34:41], v[150:153]
	v_mfma_f32_16x16x128_f8f6f4 v[146:149], v[10:17], v[34:41], v[146:149]
	s_waitcnt lgkmcnt(4)
	v_mfma_f32_16x16x128_f8f6f4 v[134:137], v[2:9], v[42:49], v[134:137]
	v_mfma_f32_16x16x128_f8f6f4 v[130:133], v[10:17], v[42:49], v[130:133]
	s_waitcnt lgkmcnt(2)
	v_mfma_f32_16x16x128_f8f6f4 v[118:121], v[2:9], v[50:57], v[118:121]
	v_mfma_f32_16x16x128_f8f6f4 v[114:117], v[10:17], v[50:57], v[114:117]
	s_waitcnt lgkmcnt(0)
	v_mfma_f32_16x16x128_f8f6f4 v[102:105], v[2:9], v[58:65], v[102:105]
	v_mfma_f32_16x16x128_f8f6f4 v[98:101], v[10:17], v[58:65], v[98:101]
	v_mfma_f32_16x16x128_f8f6f4 v[158:161], v[18:25], v[34:41], v[158:161]
	v_mfma_f32_16x16x128_f8f6f4 v[154:157], v[26:33], v[34:41], v[154:157]
	v_mfma_f32_16x16x128_f8f6f4 v[142:145], v[18:25], v[42:49], v[142:145]
	v_mfma_f32_16x16x128_f8f6f4 v[138:141], v[26:33], v[42:49], v[138:141]
	v_mfma_f32_16x16x128_f8f6f4 v[126:129], v[18:25], v[50:57], v[126:129]
	v_mfma_f32_16x16x128_f8f6f4 v[122:125], v[26:33], v[50:57], v[122:125]
	v_mfma_f32_16x16x128_f8f6f4 v[110:113], v[18:25], v[58:65], v[110:113]
	v_mfma_f32_16x16x128_f8f6f4 v[106:109], v[26:33], v[58:65], v[106:109]
	s_setprio 0
	s_barrier
	ds_read_b128 v[42:45], v169 offset:49152
	ds_read_b128 v[46:49], v169 offset:50176
	ds_read_b128 v[58:61], v169 offset:51200
	ds_read_b128 v[62:65], v169 offset:52224
	ds_read_b128 v[170:173], v169 offset:53248
	ds_read_b128 v[174:177], v169 offset:54272
	ds_read_b128 v[178:181], v169 offset:55296
	ds_read_b128 v[182:185], v169 offset:56320
	s_add_i32 s38, s74, 0x18000
	s_mov_b32 m0, s38
	s_nop 0
	global_load_lds_dwordx4 v166, s[36:37]
	s_add_i32 s38, s74, 0x1a000
	s_mov_b32 m0, s38
	s_nop 0
	global_load_lds_dwordx4 v167, s[36:37]
	s_add_u32 s34, s34, 0x2080
	s_addc_u32 s35, s35, 0
	s_add_i32 s36, s74, 0x1c000
	s_mov_b32 m0, s36
	s_nop 0
	global_load_lds_dwordx4 v166, s[34:35]
	s_add_i32 s36, s74, 0x1e000
	s_mov_b32 m0, s36
	s_nop 0
	global_load_lds_dwordx4 v167, s[34:35]
	s_waitcnt vmcnt(6)
	s_waitcnt lgkmcnt(0)
	s_barrier
; #define PG8_STAGEA1(bufoff, gbase) do { if constexpr (Sched::GATHER) { PG8_STAGEA(bufoff, gbase, vA2, vA3); } else { PG8_STAGEA(bufoff, (gbase) + hstep, vA0, vA1); } } while (0)
; #define PG8_LDA(dst, b, h) do { if constexpr (F8) { _Pragma("unroll") for (int m = 0; m < 4; ++m) dst##8[m] = PG8_LD32(lds + PG8_SA(b, h) + aoff + m * 2048); } else { \
;         _Pragma("unroll") for (int m = 0; m < 4; ++m) _Pragma("unroll") for (int k = 0; k < 2; ++k) dst[m][k] = *(const LAS bf16x8*)(lds + PG8_SA(b, h) + aoff + m * 2048 + k * 1024); } } while (0)
; #define PG8_LDB(dst, b, h) do { if constexpr (F8) { _Pragma("unroll") for (int n = 0; n < 2; ++n) dst##8[n] = PG8_LD32(lds + PG8_SB(b, h) + boff + n * 2048); } else { \
;         _Pragma("unroll") for (int n = 0; n < 2; ++n) _Pragma("unroll") for (int k = 0; k < 2; ++k) dst[n][k] = *(const LAS bf16x8*)(lds + PG8_SB(b, h) + boff + n * 2048 + k * 1024); } } while (0)
; #define PG8_WAIT_VX() do { if (relax) asm volatile("s_waitcnt vmcnt(%0)" :: "n"(8 + Epi::RELAX) : "memory"); else PG8_WAIT_V(8); } while (0)
; #define PG8_WAIT_L(n) asm volatile("s_waitcnt lgkmcnt(" #n ")" ::: "memory")
; #define PG8_BAR __builtin_amdgcn_s_barrier()
; #define PG8_SCHED __builtin_amdgcn_sched_barrier(0)
; template <class Epi, class Sched, bool F8 = false, bool PF = false, bool I8 = false, int PID = -1>
; __device__ __forceinline__ void gemm_phase(LAS unsigned char* lds, LAS unsigned char* xlds, const int RP, const int RPB, const int nt, const Sched& S, const Epi& E, const int stagger_ticks) {
;     ...
;             PG8_LDB(B0, 0, 0); PG8_LDB(B1, 0, 1); PG8_SCHED; PG8_LDA(At, 0, 0); PG8_STAGEA1(PG8_SA(1, 1), a1);
;             if (Sched::GATHER) { if (last) { const u32x4 nv = *nslot; vA0 = nv.x; vA1 = nv.y; vA2 = nv.z; vA3 = nv.w; } }
;             PG8_WAIT_VX(); PG8_WAIT_L(0); PG8_BAR; PG8_MMA(0, 0, At, B0); PG8_MMA(0, 1, At, B1); PG8_BAR; PG8_SCHED;
;             if constexpr (Epi::BIAS_DMA) { if (t == 0 && has_next) E.bias_dma(nxt, xlds + 8192 + ((ui + 1) & 1) * Epi::BIAS_STRIDE, wid, lane); }
	s_setprio 1
	s_waitcnt lgkmcnt(6)
	v_mfma_f32_16x16x128_f8f6f4 v[86:89], v[2:9], v[42:49], v[86:89]
	v_mfma_f32_16x16x128_f8f6f4 v[82:85], v[10:17], v[42:49], v[82:85]
	s_waitcnt lgkmcnt(4)
	v_mfma_f32_16x16x128_f8f6f4 v[70:73], v[2:9], v[58:65], v[70:73]
	v_mfma_f32_16x16x128_f8f6f4 v[66:69], v[10:17], v[58:65], v[66:69]
	s_waitcnt lgkmcnt(2)
	v_mfma_f32_16x16x128_f8f6f4 v[54:57], v[2:9], v[170:177], v[202:205]
	v_mfma_f32_16x16x128_f8f6f4 v[50:53], v[10:17], v[170:177], v[206:209]
	s_waitcnt lgkmcnt(0)
	v_mfma_f32_16x16x128_f8f6f4 v[38:41], v[2:9], v[178:185], v[210:213]
	v_mfma_f32_16x16x128_f8f6f4 v[34:37], v[10:17], v[178:185], v[214:217]
	v_mfma_f32_16x16x128_f8f6f4 v[94:97], v[18:25], v[42:49], v[94:97]
	v_mfma_f32_16x16x128_f8f6f4 v[90:93], v[26:33], v[42:49], v[90:93]
	v_mfma_f32_16x16x128_f8f6f4 v[78:81], v[18:25], v[58:65], v[78:81]
	v_mfma_f32_16x16x128_f8f6f4 v[74:77], v[26:33], v[58:65], v[74:77]
	v_mfma_f32_16x16x128_f8f6f4 v[62:65], v[18:25], v[170:177], v[218:221]
	v_mfma_f32_16x16x128_f8f6f4 v[58:61], v[26:33], v[170:177], v[186:189]
	v_mfma_f32_16x16x128_f8f6f4 v[46:49], v[18:25], v[178:185], v[190:193]
	v_mfma_f32_16x16x128_f8f6f4 v[42:45], v[26:33], v[178:185], v[194:197]
	s_setprio 0
	s_barrier
	s_add_i32 s73, s73, 2
	s_add_u32 s25, s25, 0x100
	s_addc_u32 s71, s71, 0
	s_add_u32 s26, s26, 0x100
	s_addc_u32 s27, s27, 0
	s_cmp_gt_u32 s73, 5
	s_cbranch_scc1 .LBB0_1065
.LBB0_1063:
	s_mov_b32 s74, s47
	s_add_u32 s100, s26, 0xfffe0000
	s_addc_u32 s101, s27, -1
	s_add_i32 s30, s74, 0x8000
	s_mov_b32 m0, s30
	s_nop 0
	global_load_lds_dwordx4 v164, s[100:101]
	s_add_i32 s30, s74, 0xa000
	s_mov_b32 m0, s30
	s_nop 0
	global_load_lds_dwordx4 v165, s[100:101]
	v_add_u32_e32 v14, 0x10000, v168
	v_add_u32_e32 v30, 0x14000, v168
	ds_read_b128 v[2:5], v14
	ds_read_b128 v[6:9], v14 offset:1024
	ds_read_b128 v[10:13], v14 offset:2048
	ds_read_b128 v[14:17], v14 offset:3072
	ds_read_b128 v[18:21], v30
	ds_read_b128 v[22:25], v30 offset:1024
	ds_read_b128 v[26:29], v30 offset:2048
	ds_read_b128 v[30:33], v30 offset:3072
	ds_read_b128 v[170:173], v169
	ds_read_b128 v[174:177], v169 offset:1024
	ds_read_b128 v[178:181], v169 offset:2048
	ds_read_b128 v[182:185], v169 offset:3072
	ds_read_b128 v[186:189], v169 offset:4096
	ds_read_b128 v[190:193], v169 offset:5120
	ds_read_b128 v[194:197], v169 offset:6144
	ds_read_b128 v[198:201], v169 offset:7168
	s_add_i32 s30, s74, 0xc000
	s_mov_b32 m0, s30
	s_nop 0
	global_load_lds_dwordx4 v164, s[26:27]
	s_add_i32 s30, s74, 0xe000
	s_mov_b32 m0, s30
	s_nop 0
	global_load_lds_dwordx4 v165, s[26:27]
	s_waitcnt vmcnt(8)
	s_waitcnt lgkmcnt(0)
	s_barrier
	s_setprio 1
	s_waitcnt lgkmcnt(6)
	v_mfma_f32_16x16x128_f8f6f4 v[150:153], v[2:9], v[170:177], v[150:153]
	v_mfma_f32_16x16x128_f8f6f4 v[146:149], v[10:17], v[170:177], v[146:149]
	s_waitcnt lgkmcnt(4)
	v_mfma_f32_16x16x128_f8f6f4 v[134:137], v[2:9], v[178:185], v[134:137]
	v_mfma_f32_16x16x128_f8f6f4 v[130:133], v[10:17], v[178:185], v[130:133]
	s_waitcnt lgkmcnt(2)
	v_mfma_f32_16x16x128_f8f6f4 v[118:121], v[2:9], v[186:193], v[118:121]
	v_mfma_f32_16x16x128_f8f6f4 v[114:117], v[10:17], v[186:193], v[114:117]
	s_waitcnt lgkmcnt(0)
	v_mfma_f32_16x16x128_f8f6f4 v[102:105], v[2:9], v[194:201], v[102:105]
	v_mfma_f32_16x16x128_f8f6f4 v[98:101], v[10:17], v[194:201], v[98:101]
	v_mfma_f32_16x16x128_f8f6f4 v[158:161], v[18:25], v[170:177], v[158:161]
	v_mfma_f32_16x16x128_f8f6f4 v[154:157], v[26:33], v[170:177], v[154:157]
	v_mfma_f32_16x16x128_f8f6f4 v[142:145], v[18:25], v[178:185], v[142:145]
	v_mfma_f32_16x16x128_f8f6f4 v[138:141], v[26:33], v[178:185], v[138:141]
	v_mfma_f32_16x16x128_f8f6f4 v[126:129], v[18:25], v[186:193], v[126:129]
	v_mfma_f32_16x16x128_f8f6f4 v[122:125], v[26:33], v[186:193], v[122:125]
	v_mfma_f32_16x16x128_f8f6f4 v[110:113], v[18:25], v[194:201], v[110:113]
	v_mfma_f32_16x16x128_f8f6f4 v[106:109], v[26:33], v[194:201], v[106:109]
	s_setprio 0
	s_barrier
	s_cmp_lg_u32 s73, -2
	s_cselect_b64 s[30:31], -1, 0
	s_or_b64 s[30:31], s[30:31], s[28:29]
	s_and_b64 vcc, exec, s[30:31]
	s_cbranch_vccnz .LBB0_1062
	s_mov_b32 m0, s72
	s_nop 0
	global_load_lds_dword v1, s[2:3]
	s_branch .LBB0_1062
.Lmy_z8t:
	s_mov_b32 s74, s47
	s_add_u32 s100, s26, 0xfffe0000
	s_addc_u32 s101, s27, -1
	s_add_i32 s30, s74, 0x8000
	s_mov_b32 m0, s30
	s_nop 0
	global_load_lds_dwordx4 v164, s[100:101]
	s_add_i32 s30, s74, 0xa000
	s_mov_b32 m0, s30
	s_nop 0
	global_load_lds_dwordx4 v165, s[100:101]
	v_add_u32_e32 v14, 0x10000, v168
	v_add_u32_e32 v30, 0x14000, v168
	ds_read_b128 v[2:5], v14
	ds_read_b128 v[6:9], v14 offset:1024
	ds_read_b128 v[10:13], v14 offset:2048
	ds_read_b128 v[14:17], v14 offset:3072
	ds_read_b128 v[18:21], v30
	ds_read_b128 v[22:25], v30 offset:1024
	ds_read_b128 v[26:29], v30 offset:2048
	ds_read_b128 v[30:33], v30 offset:3072
	ds_read_b128 v[170:173], v169
	ds_read_b128 v[174:177], v169 offset:1024
	ds_read_b128 v[178:181], v169 offset:2048
	ds_read_b128 v[182:185], v169 offset:3072
	ds_read_b128 v[186:189], v169 offset:4096
	ds_read_b128 v[190:193], v169 offset:5120
	ds_read_b128 v[194:197], v169 offset:6144
	ds_read_b128 v[198:201], v169 offset:7168
	s_add_i32 s30, s74, 0xc000
	s_mov_b32 m0, s30
	s_nop 0
	global_load_lds_dwordx4 v164, s[26:27]
	s_add_i32 s30, s74, 0xe000
	s_mov_b32 m0, s30
	s_nop 0
	global_load_lds_dwordx4 v165, s[26:27]
	s_waitcnt vmcnt(8)
	s_waitcnt lgkmcnt(0)
	s_barrier
	s_setprio 1
	s_waitcnt lgkmcnt(6)
	v_mfma_f32_16x16x128_f8f6f4 v[150:153], v[2:9], v[170:177], 0
	v_mfma_f32_16x16x128_f8f6f4 v[146:149], v[10:17], v[170:177], 0
	s_waitcnt lgkmcnt(4)
	v_mfma_f32_16x16x128_f8f6f4 v[134:137], v[2:9], v[178:185], 0
	v_mfma_f32_16x16x128_f8f6f4 v[130:133], v[10:17], v[178:185], 0
	s_waitcnt lgkmcnt(2)
	v_mfma_f32_16x16x128_f8f6f4 v[118:121], v[2:9], v[186:193], 0
	v_mfma_f32_16x16x128_f8f6f4 v[114:117], v[10:17], v[186:193], 0
	s_waitcnt lgkmcnt(0)
	v_mfma_f32_16x16x128_f8f6f4 v[102:105], v[2:9], v[194:201], 0
	v_mfma_f32_16x16x128_f8f6f4 v[98:101], v[10:17], v[194:201], 0
	v_mfma_f32_16x16x128_f8f6f4 v[158:161], v[18:25], v[170:177], 0
	v_mfma_f32_16x16x128_f8f6f4 v[154:157], v[26:33], v[170:177], 0
	v_mfma_f32_16x16x128_f8f6f4 v[142:145], v[18:25], v[178:185], 0
	v_mfma_f32_16x16x128_f8f6f4 v[138:141], v[26:33], v[178:185], 0
	v_mfma_f32_16x16x128_f8f6f4 v[126:129], v[18:25], v[186:193], 0
	v_mfma_f32_16x16x128_f8f6f4 v[122:125], v[26:33], v[186:193], 0
	v_mfma_f32_16x16x128_f8f6f4 v[110:113], v[18:25], v[194:201], 0
	v_mfma_f32_16x16x128_f8f6f4 v[106:109], v[26:33], v[194:201], 0
	s_setprio 0
	s_barrier
	s_cmp_lg_u32 s73, -2
	s_cselect_b64 s[30:31], -1, 0
	s_or_b64 s[30:31], s[30:31], s[28:29]
	s_and_b64 vcc, exec, s[30:31]
	s_cbranch_vccnz .Lmy_z8b
	s_mov_b32 m0, s72
	s_nop 0
	global_load_lds_dword v1, s[2:3]
	s_branch .Lmy_z8b
; #define PG8_STAGE(bufoff, gbase, voff) do { PG8_GLDS((const char*)(gbase), (voff)[0], ldsb + (bufoff)); PG8_GLDS((const char*)(gbase), (voff)[1], ldsb + (bufoff) + 8192u); } while (0)
; #define PG8_STAGEA(bufoff, gbase, o0, o1) do { PG8_GLDS((const char*)(gbase), (o0), ldsb + (bufoff)); PG8_GLDS((const char*)(gbase), (o1), ldsb + (bufoff) + 8192u); } while (0)
; #define PG8_STAGEA1(bufoff, gbase) do { if constexpr (Sched::GATHER) { PG8_STAGEA(bufoff, gbase, vA2, vA3); } else { PG8_STAGEA(bufoff, (gbase) + hstep, vA0, vA1); } } while (0)
; #define PG8_LDA(dst, b, h) do { if constexpr (F8) { _Pragma("unroll") for (int m = 0; m < 4; ++m) dst##8[m] = PG8_LD32(lds + PG8_SA(b, h) + aoff + m * 2048); } else { \
;         _Pragma("unroll") for (int m = 0; m < 4; ++m) _Pragma("unroll") for (int k = 0; k < 2; ++k) dst[m][k] = *(const LAS bf16x8*)(lds + PG8_SA(b, h) + aoff + m * 2048 + k * 1024); } } while (0)
; #define PG8_LDB(dst, b, h) do { if constexpr (F8) { _Pragma("unroll") for (int n = 0; n < 2; ++n) dst##8[n] = PG8_LD32(lds + PG8_SB(b, h) + boff + n * 2048); } else { \
;         _Pragma("unroll") for (int n = 0; n < 2; ++n) _Pragma("unroll") for (int k = 0; k < 2; ++k) dst[n][k] = *(const LAS bf16x8*)(lds + PG8_SB(b, h) + boff + n * 2048 + k * 1024); } } while (0)
; #define PG8_WAIT_VR() PG8_WAIT_V(8)
; template <class Epi, class Sched, bool F8 = false, bool PF = false, bool I8 = false, int PID = -1>
; __device__ __forceinline__ void gemm_phase(LAS unsigned char* lds, LAS unsigned char* xlds, const int RP, const int RPB, const int nt, const Sched& S, const Epi& E, const int stagger_ticks) {
;     ...
;             PG8_LDA(At, 0, 1); PG8_STAGE(PG8_SB(0, 0), b2, voffB); PG8_STAGE(PG8_SB(0, 1), b2 + hstepB, voffB); PG8_STAGEA(PG8_SA(0, 0), a2, vA0, vA1);
;             PG8_WAIT_VX(); PG8_WAIT_L(0); PG8_BAR; PG8_MMA(1, 0, At, B0); PG8_MMA(1, 1, At, B1); PG8_BAR; PG8_SCHED;
;             PG8_LDB(B0, 1, 0); PG8_LDB(B1, 1, 1); PG8_SCHED; PG8_LDA(At, 1, 0); PG8_STAGEA1(PG8_SA(0, 1), a2);
;             PG8_WAIT_VR(); PG8_WAIT_L(0); PG8_BAR; PG8_MMA(0, 0, At, B0); PG8_MMA(0, 1, At, B1); PG8_BAR; PG8_SCHED;
;             PG8_LDA(At, 1, 1); PG8_STAGE(PG8_SB(1, 0), b3, voffB); PG8_STAGE(PG8_SB(1, 1), b3 + hstepB, voffB); PG8_STAGEA(PG8_SA(1, 0), a3, vA0, vA1);
;             PG8_WAIT_VR(); PG8_WAIT_L(0); PG8_BAR; PG8_MMA(1, 0, At, B0); PG8_MMA(1, 1, At, B1); PG8_BAR; PG8_SCHED;
.Lmy_z8b:
	s_add_u32 s30, s26, 0xfffe0080
	s_addc_u32 s31, s27, -1
	s_cmp_eq_u32 s73, 4
	s_cselect_b32 s38, s6, s30
	s_cselect_b32 s39, s7, s31
	s_cselect_b32 s34, s8, s25
	s_cselect_b32 s35, s9, s71
	s_add_u32 s30, s38, 0x80
	s_addc_u32 s31, s39, 0
	s_add_u32 s36, s34, 0x80
	s_addc_u32 s37, s35, 0
	ds_read_b128 v[170:173], v169 offset:16384
	ds_read_b128 v[174:177], v169 offset:17408
	ds_read_b128 v[178:181], v169 offset:18432
	ds_read_b128 v[182:185], v169 offset:19456
	ds_read_b128 v[186:189], v169 offset:20480
	ds_read_b128 v[190:193], v169 offset:21504
	ds_read_b128 v[194:197], v169 offset:22528
	ds_read_b128 v[198:201], v169 offset:23552
	s_add_i32 s75, s74, 0x10000
	s_mov_b32 m0, s75
	s_nop 0
	global_load_lds_dwordx4 v166, s[34:35]
	s_add_i32 s75, s74, 0x12000
	s_mov_b32 m0, s75
	s_nop 0
	global_load_lds_dwordx4 v167, s[34:35]
	s_add_u32 s76, s34, 0x2000
	s_addc_u32 s77, s35, 0
	s_add_i32 s75, s74, 0x14000
	s_mov_b32 m0, s75
	s_nop 0
	global_load_lds_dwordx4 v166, s[76:77]
	s_add_i32 s75, s74, 0x16000
	s_mov_b32 m0, s75
	s_nop 0
	global_load_lds_dwordx4 v167, s[76:77]
	s_waitcnt vmcnt(6)
	s_waitcnt lgkmcnt(0)
	s_barrier
	s_setprio 1
	s_waitcnt lgkmcnt(6)
	v_mfma_f32_16x16x128_f8f6f4 v[86:89], v[2:9], v[170:177], 0
	v_mfma_f32_16x16x128_f8f6f4 v[82:85], v[10:17], v[170:177], 0
	s_waitcnt lgkmcnt(4)
	v_mfma_f32_16x16x128_f8f6f4 v[70:73], v[2:9], v[178:185], 0
	v_mfma_f32_16x16x128_f8f6f4 v[66:69], v[10:17], v[178:185], 0
	s_waitcnt lgkmcnt(2)
	v_mfma_f32_16x16x128_f8f6f4 v[202:205], v[2:9], v[186:193], 0
	v_mfma_f32_16x16x128_f8f6f4 v[206:209], v[10:17], v[186:193], 0
	s_waitcnt lgkmcnt(0)
	v_mfma_f32_16x16x128_f8f6f4 v[210:213], v[2:9], v[194:201], 0
	v_mfma_f32_16x16x128_f8f6f4 v[214:217], v[10:17], v[194:201], 0
	v_mfma_f32_16x16x128_f8f6f4 v[94:97], v[18:25], v[170:177], 0
	v_mfma_f32_16x16x128_f8f6f4 v[90:93], v[26:33], v[170:177], 0
	v_mfma_f32_16x16x128_f8f6f4 v[78:81], v[18:25], v[178:185], 0
	v_mfma_f32_16x16x128_f8f6f4 v[74:77], v[26:33], v[178:185], 0
	v_mfma_f32_16x16x128_f8f6f4 v[218:221], v[18:25], v[186:193], 0
	v_mfma_f32_16x16x128_f8f6f4 v[186:189], v[26:33], v[186:193], 0
	v_mfma_f32_16x16x128_f8f6f4 v[190:193], v[18:25], v[194:201], 0
	v_mfma_f32_16x16x128_f8f6f4 v[194:197], v[26:33], v[194:201], 0
	s_setprio 0
	s_barrier
	s_add_i32 s75, s74, 0x2000
	s_mov_b32 m0, s74
	s_nop 0
	global_load_lds_dwordx4 v164, s[38:39]
	s_nop 0
	s_mov_b32 m0, s75
	s_nop 0
	global_load_lds_dwordx4 v165, s[38:39]
	v_add_u32_e32 v14, 0x18000, v168
	v_add_u32_e32 v30, 0x1c000, v168
	ds_read_b128 v[2:5], v14
	ds_read_b128 v[6:9], v14 offset:1024
	ds_read_b128 v[10:13], v14 offset:2048
	ds_read_b128 v[14:17], v14 offset:3072
	ds_read_b128 v[18:21], v30
	ds_read_b128 v[22:25], v30 offset:1024
	ds_read_b128 v[26:29], v30 offset:2048
	ds_read_b128 v[30:33], v30 offset:3072
	ds_read_b128 v[34:37], v169 offset:32768
	ds_read_b128 v[38:41], v169 offset:33792
	ds_read_b128 v[42:45], v169 offset:34816
	ds_read_b128 v[46:49], v169 offset:35840
	ds_read_b128 v[50:53], v169 offset:36864
	ds_read_b128 v[54:57], v169 offset:37888
	ds_read_b128 v[58:61], v169 offset:38912
	ds_read_b128 v[62:65], v169 offset:39936
	s_add_u32 s38, s38, 0x20000
	s_addc_u32 s39, s39, 0
	s_add_i32 s75, s74, 0x4000
	s_mov_b32 m0, s75
	s_nop 0
	global_load_lds_dwordx4 v164, s[38:39]
	s_add_i32 s75, s74, 0x6000
	s_mov_b32 m0, s75
	s_nop 0
	global_load_lds_dwordx4 v165, s[38:39]
	s_waitcnt vmcnt(8)
	s_waitcnt lgkmcnt(0)
	s_barrier
	s_setprio 1
	s_waitcnt lgkmcnt(6)
	v_mfma_f32_16x16x128_f8f6f4 v[150:153], v[2:9], v[34:41], v[150:153]
	v_mfma_f32_16x16x128_f8f6f4 v[146:149], v[10:17], v[34:41], v[146:149]
	s_waitcnt lgkmcnt(4)
	v_mfma_f32_16x16x128_f8f6f4 v[134:137], v[2:9], v[42:49], v[134:137]
	v_mfma_f32_16x16x128_f8f6f4 v[130:133], v[10:17], v[42:49], v[130:133]
	s_waitcnt lgkmcnt(2)
	v_mfma_f32_16x16x128_f8f6f4 v[118:121], v[2:9], v[50:57], v[118:121]
	v_mfma_f32_16x16x128_f8f6f4 v[114:117], v[10:17], v[50:57], v[114:117]
	s_waitcnt lgkmcnt(0)
	v_mfma_f32_16x16x128_f8f6f4 v[102:105], v[2:9], v[58:65], v[102:105]
	v_mfma_f32_16x16x128_f8f6f4 v[98:101], v[10:17], v[58:65], v[98:101]
	v_mfma_f32_16x16x128_f8f6f4 v[158:161], v[18:25], v[34:41], v[158:161]
	v_mfma_f32_16x16x128_f8f6f4 v[154:157], v[26:33], v[34:41], v[154:157]
	v_mfma_f32_16x16x128_f8f6f4 v[142:145], v[18:25], v[42:49], v[142:145]
	v_mfma_f32_16x16x128_f8f6f4 v[138:141], v[26:33], v[42:49], v[138:141]
	v_mfma_f32_16x16x128_f8f6f4 v[126:129], v[18:25], v[50:57], v[126:129]
	v_mfma_f32_16x16x128_f8f6f4 v[122:125], v[26:33], v[50:57], v[122:125]
	v_mfma_f32_16x16x128_f8f6f4 v[110:113], v[18:25], v[58:65], v[110:113]
	v_mfma_f32_16x16x128_f8f6f4 v[106:109], v[26:33], v[58:65], v[106:109]
	s_setprio 0
	s_barrier
	ds_read_b128 v[42:45], v169 offset:49152
	ds_read_b128 v[46:49], v169 offset:50176
	ds_read_b128 v[58:61], v169 offset:51200
	ds_read_b128 v[62:65], v169 offset:52224
	ds_read_b128 v[170:173], v169 offset:53248
	ds_read_b128 v[174:177], v169 offset:54272
	ds_read_b128 v[178:181], v169 offset:55296
	ds_read_b128 v[182:185], v169 offset:56320
	s_add_i32 s38, s74, 0x18000
	s_mov_b32 m0, s38
	s_nop 0
	global_load_lds_dwordx4 v166, s[36:37]
	s_add_i32 s38, s74, 0x1a000
	s_mov_b32 m0, s38
	s_nop 0
	global_load_lds_dwordx4 v167, s[36:37]
	s_add_u32 s34, s34, 0x2080
	s_addc_u32 s35, s35, 0
	s_add_i32 s36, s74, 0x1c000
	s_mov_b32 m0, s36
	s_nop 0
	global_load_lds_dwordx4 v166, s[34:35]
	s_add_i32 s36, s74, 0x1e000
	s_mov_b32 m0, s36
	s_nop 0
	global_load_lds_dwordx4 v167, s[34:35]
	s_waitcnt vmcnt(6)
	s_waitcnt lgkmcnt(0)
	s_barrier
	s_setprio 1
	s_waitcnt lgkmcnt(6)
	v_mfma_f32_16x16x128_f8f6f4 v[86:89], v[2:9], v[42:49], v[86:89]
	v_mfma_f32_16x16x128_f8f6f4 v[82:85], v[10:17], v[42:49], v[82:85]
	s_waitcnt lgkmcnt(4)
	v_mfma_f32_16x16x128_f8f6f4 v[70:73], v[2:9], v[58:65], v[70:73]
	v_mfma_f32_16x16x128_f8f6f4 v[66:69], v[10:17], v[58:65], v[66:69]
	s_waitcnt lgkmcnt(2)
	v_mfma_f32_16x16x128_f8f6f4 v[54:57], v[2:9], v[170:177], v[202:205]
	v_mfma_f32_16x16x128_f8f6f4 v[50:53], v[10:17], v[170:177], v[206:209]
	s_waitcnt lgkmcnt(0)
	v_mfma_f32_16x16x128_f8f6f4 v[38:41], v[2:9], v[178:185], v[210:213]
	v_mfma_f32_16x16x128_f8f6f4 v[34:37], v[10:17], v[178:185], v[214:217]
	v_mfma_f32_16x16x128_f8f6f4 v[94:97], v[18:25], v[42:49], v[94:97]
	v_mfma_f32_16x16x128_f8f6f4 v[90:93], v[26:33], v[42:49], v[90:93]
	v_mfma_f32_16x16x128_f8f6f4 v[78:81], v[18:25], v[58:65], v[78:81]
	v_mfma_f32_16x16x128_f8f6f4 v[74:77], v[26:33], v[58:65], v[74:77]
	v_mfma_f32_16x16x128_f8f6f4 v[62:65], v[18:25], v[170:177], v[218:221]
	v_mfma_f32_16x16x128_f8f6f4 v[58:61], v[26:33], v[170:177], v[186:189]
	v_mfma_f32_16x16x128_f8f6f4 v[46:49], v[18:25], v[178:185], v[190:193]
	v_mfma_f32_16x16x128_f8f6f4 v[42:45], v[26:33], v[178:185], v[194:197]
	s_setprio 0
	s_barrier
	s_add_i32 s73, s73, 2
	s_add_u32 s25, s25, 0x100
	s_addc_u32 s71, s71, 0
	s_add_u32 s26, s26, 0x100
	s_addc_u32 s27, s27, 0
	s_cmp_gt_u32 s73, 5
	s_branch .LBB0_1063
